# GDN chunk unit fetch2: running 64-bit pointers (one add per gather) instead of per-gather address recomputation, single wave-role split, counted waits for the prefetched operands
# speedup vs baseline: 1.0129x; 1.0074x over previous
; __device__ __forceinline__ void gdn_fetch(CArgs& a, int u, int w, int lane, GdnIn& in) {
;     const int chain = u / 36, n = u % 36, b = chain >> 3, h = (chain >> 1) & 3, dir = chain & 1;
;     const int r0 = scan_row(b, dir, n * 64), step = dir ? -1 : 1, fr = lane & 15, kg = lane >> 4;
;     const float* DQ = (const float*)(a.ws + WS_MIX + MX_DQ) + h * 64; const float* DK = (const float*)(a.ws + WS_MIX + MX_DK) + h * 64; const float* DV = (const float*)(a.ws + WS_MIX + MX_DV) + h * 64;
;     const float* DG = (const float*)(a.ws + WS_MIX + MX_DG);
;     const bf16* KB = (const bf16*)(a.ws + WS_CKD + CD_KB) + (ptrdiff_t)r0 * 256 + h * 64; const bf16* QB = (const bf16*)(a.ws + WS_CKD + CD_QB) + (ptrdiff_t)r0 * 256 + h * 64;
;     const ptrdiff_t ldt = (ptrdiff_t)step * 256;
;     const bool isW = w >= 4; const int c0 = 16 * (w & 3), I1 = w >> 1;
;     in.g2 = *(const f32x2*)(DG + (size_t)(r0 + step * lane) * 16 + h * 4 + dir * 2);
; #pragma unroll
;     for (int s = 0; s < 2; ++s) { in.ak[s] = *(const bf16x8*)(KB + (ptrdiff_t)(16 * I1 + fr) * ldt + 32 * s + 8 * kg); in.aq[s] = *(const bf16x8*)(QB + (ptrdiff_t)(16 * I1 + fr) * ldt + 32 * s + 8 * kg);
; #pragma unroll
;         for (int jj = 0; jj < 2; ++jj) in.bk[jj][s] = *(const bf16x8*)(KB + (ptrdiff_t)(16 * (2 * (w & 1) + jj) + fr) * ldt + 32 * s + 8 * kg); }
; #pragma unroll
;     for (int tt = 0; tt < 8; ++tt) in.kt8[tt] = KB[(ptrdiff_t)(8 * w + tt) * ldt + lane];
; }
.LBB0_1680:
	s_and_b64 vcc, exec, s[2:3]
	s_cbranch_vccz .LBB0_1798
	v_readlane_b32 s9, v248, 37
	s_bfe_i32 s2, s9, 0x10000
	s_lshl_b32 s3, s9, 5
	s_and_b32 s3, s3, 0xffffff00
	s_and_b32 s2, s2, 0xff
	s_or_b32 s26, s2, s3
	s_ashr_i32 s27, s26, 31
	s_and_b32 s0, s9, 1
	s_bfe_u32 s9, s9, 0x20001
	s_lshl_b64 s[28:29], s[26:27], 9
	v_readlane_b32 s2, v251, 14
	s_add_u32 s2, s2, s28
	v_readlane_b32 s3, v249, 10
	s_addc_u32 s3, s3, s29
	s_lshl_b32 s20, s9, 7
	s_add_u32 s2, s2, s20
	s_addc_u32 s3, s3, 0
	s_add_u32 s27, s37, s28
	s_addc_u32 s29, s72, s29
	s_add_u32 s28, s27, s20
	s_addc_u32 s29, s29, 0
	s_cmp_eq_u32 s0, 0
	v_mov_b32_e32 v110, v160
	s_cselect_b32 s20, 1, -1
	s_movk_i32 s27, 0xff00
	s_waitcnt vmcnt(0)
	v_mul_lo_u32 v2, v110, s20
	v_add_u32_e32 v2, s26, v2
	v_ashrrev_i32_e32 v3, 31, v2
	v_lshlrev_b64 v[2:3], 6, v[2:3]
	s_cselect_b32 s36, 0x100, s27
	v_lshl_add_u64 v[2:3], s[6:7], 0, v[2:3]
	s_lshl_b32 s78, s9, 4
	v_lshl_add_u64 v[2:3], v[2:3], 0, s[78:79]
	s_lshl_b32 s78, s0, 3
	v_and_b32_e32 v1, 15, v110
	v_lshl_add_u64 v[2:3], v[2:3], 0, s[78:79]
	v_ashrrev_i32_e32 v6, 1, v110
	global_load_dwordx2 v[112:113], v[2:3], off
	v_or_b32_e32 v2, s42, v1
	v_and_b32_e32 v6, -8, v6
	v_mad_i64_i32 v[2:3], s[26:27], s36, v2, 0
	v_ashrrev_i32_e32 v7, 31, v6
	v_or_b32_e32 v1, s43, v1
	v_lshlrev_b64 v[2:3], 1, v[2:3]
	v_lshlrev_b64 v[6:7], 1, v[6:7]
	v_mul_hi_i32_i24_e32 v11, s36, v1
	v_mul_i32_i24_e32 v10, s36, v1
	v_or_b32_e32 v1, 16, v1
	v_lshl_add_u64 v[4:5], s[2:3], 0, v[2:3]
	v_lshl_add_u64 v[2:3], s[28:29], 0, v[2:3]
	v_lshl_add_u64 v[14:15], s[2:3], 0, v[6:7]
	v_mul_hi_i32_i24_e32 v17, s36, v1
	v_mul_i32_i24_e32 v16, s36, v1
	v_ashrrev_i32_e32 v111, 31, v110
	v_lshl_add_u64 v[18:19], v[4:5], 0, v[6:7]
	v_lshl_add_u64 v[22:23], v[2:3], 0, v[6:7]
	v_lshl_add_u64 v[26:27], v[10:11], 1, v[14:15]
	v_lshl_add_u64 v[30:31], v[16:17], 1, v[14:15]
	v_lshl_add_u64 v[32:33], v[110:111], 1, s[2:3]
	s_mul_hi_i32 s3, s36, s73
	s_mul_i32 s2, s36, s73
	global_load_dwordx4 v[2:5], v[18:19], off
	global_load_dwordx4 v[6:9], v[22:23], off
	global_load_dwordx4 v[10:13], v[26:27], off
	global_load_dwordx4 v[14:17], v[30:31], off
	s_nop 0
	global_load_dwordx4 v[18:21], v[18:19], off offset:64
	s_nop 0
	global_load_dwordx4 v[22:25], v[22:23], off offset:64
	s_nop 0
	global_load_dwordx4 v[26:29], v[26:27], off offset:64
	s_nop 0
	global_load_dwordx4 v[36:39], v[30:31], off offset:64
	v_lshl_add_u64 v[30:31], s[2:3], 1, v[32:33]
	s_mul_hi_i32 s3, s36, s16
	s_mul_i32 s2, s36, s16
	v_lshl_add_u64 v[40:41], s[2:3], 1, v[32:33]
	s_mul_hi_i32 s3, s36, s17
	s_mul_i32 s2, s36, s17
	global_load_ushort v30, v[30:31], off
	s_mov_b32 s0, 0
	global_load_ushort v1, v[40:41], off
	v_lshl_add_u64 v[40:41], s[2:3], 1, v[32:33]
	s_mul_hi_i32 s3, s36, s35
	s_mul_i32 s2, s36, s35
	v_lshl_add_u64 v[42:43], s[2:3], 1, v[32:33]
	s_mul_hi_i32 s3, s36, s14
	s_mul_i32 s2, s36, s14
	global_load_ushort v40, v[40:41], off
	s_nop 0
	global_load_ushort v31, v[42:43], off
	v_lshl_add_u64 v[42:43], s[2:3], 1, v[32:33]
	s_mul_hi_i32 s3, s36, s82
	s_mul_i32 s2, s36, s82
	v_lshl_add_u64 v[44:45], s[2:3], 1, v[32:33]
	s_mul_hi_i32 s3, s36, s83
	s_mul_i32 s2, s36, s83
	global_load_ushort v42, v[42:43], off
	s_nop 0
	global_load_ushort v41, v[44:45], off
	v_lshl_add_u64 v[44:45], s[2:3], 1, v[32:33]
	s_mul_hi_i32 s3, s36, s10
	s_mul_i32 s2, s36, s10
	v_lshl_add_u64 v[32:33], s[2:3], 1, v[32:33]
	global_load_ushort v44, v[44:45], off
	s_nop 0
	global_load_ushort v43, v[32:33], off
	s_waitcnt vmcnt(0)
	s_branch .LBB0_1683

; __device__ __forceinline__ void gdn_fetch2(CArgs& a, int u, int w, int lane, GdnIn2& in) {
;     const int chain = u / 36, n = u % 36, b = chain >> 3, h = (chain >> 1) & 3, dir = chain & 1;
;     const int r0 = scan_row(b, dir, n * 64), step = dir ? -1 : 1, fr = lane & 15, kg = lane >> 4;
;     const bf16* QBh = (const bf16*)(a.ws + WS_CKD + CD_QB) + h * 64; const bf16* KBh = (const bf16*)(a.ws + WS_CKD + CD_KB) + h * 64; const bf16* VBh = (const bf16*)(a.ws + WS_MIX + MX_DV) + h * 64;
;     const bool isW = w >= 4; const int c0 = 16 * (w & 3);
; #pragma unroll
;     for (int I = 0; I < 4; ++I)
; #pragma unroll
;         for (int e = 0; e < 4; ++e) { const size_t ro = (size_t)(r0 + step * (16 * I + 4 * kg + e)) * 256 + c0 + fr; in.R[I][e] = isW ? (unsigned)KBh[ro] : (unsigned)VBh[ro]; in.Qv[I][e] = isW ? (unsigned)QBh[ro] : 0u; }
; }
.LBB0_1687:
	v_ashrrev_i32_e32 v46, 2, v110
	s_cmp_eq_u32 s27, 0
	v_and_b32_e32 v54, -4, v46
	v_sub_u32_e32 v32, 0, v54
	s_cselect_b64 s[48:49], -1, 0
	s_lshl_b32 s2, s20, 6
	s_and_b32 s2, s2, 0x180
	v_cndmask_b32_e64 v32, v32, v54, s[48:49]
	s_add_u32 s28, s37, s2
	v_add_u32_e32 v32, s9, v32
	v_and_b32_e32 v119, 15, v110
	s_addc_u32 s29, s72, 0
	v_ashrrev_i32_e32 v33, 31, v32
	v_or_b32_e32 v45, s68, v119
	s_add_u32 s52, s69, s2
	v_lshlrev_b64 v[32:33], 8, v[32:33]
	s_addc_u32 s53, s15, 0
	v_or_b32_e32 v32, v32, v45
	v_cndmask_b32_e64 v47, 0, 1, s[38:39]
	v_mov_b32_e32 v150, 0
	v_cmp_ne_u32_e64 s[50:51], 1, v47
	v_mov_b32_e32 v151, 0
	v_mov_b32_e32 v152, 0
	v_mov_b32_e32 v153, 0
	v_mov_b32_e32 v146, 0
	v_mov_b32_e32 v147, 0
	v_mov_b32_e32 v148, 0
	v_mov_b32_e32 v149, 0
	v_mov_b32_e32 v142, 0
	v_mov_b32_e32 v144, 0
	v_mov_b32_e32 v143, 0
	v_mov_b32_e32 v145, 0
	v_mov_b32_e32 v138, 0
	v_mov_b32_e32 v140, 0
	v_mov_b32_e32 v139, 0
	v_mov_b32_e32 v141, 0
	v_mov_b32_e32 v236, 0x200
	v_mov_b32_e32 v240, 0xfffffe00
	v_mov_b32_e32 v238, 0x1a00
	v_mov_b32_e32 v241, 0xffffe600
	v_cndmask_b32_e64 v236, v240, v236, s[48:49]
	v_cndmask_b32_e64 v238, v241, v238, s[48:49]
	v_ashrrev_i32_e32 v237, 31, v236
	v_ashrrev_i32_e32 v239, 31, v238
	v_lshl_add_u64 v[48:49], v[32:33], 1, s[52:53]
	s_andn2_b64 vcc, exec, s[38:39]
	s_cbranch_vccnz .Lgf2a_noq
	s_waitcnt vmcnt(32)
	v_lshl_add_u64 v[32:33], v[32:33], 1, s[28:29]
	global_load_ushort v34, v[48:49], off
	global_load_ushort v151, v[32:33], off
	v_lshl_add_u64 v[48:49], v[48:49], 0, v[236:237]
	v_lshl_add_u64 v[32:33], v[32:33], 0, v[236:237]
	global_load_ushort v82, v[48:49], off
	global_load_ushort v150, v[32:33], off
	v_lshl_add_u64 v[48:49], v[48:49], 0, v[236:237]
	v_lshl_add_u64 v[32:33], v[32:33], 0, v[236:237]
	global_load_ushort v83, v[48:49], off
	global_load_ushort v153, v[32:33], off
	v_lshl_add_u64 v[48:49], v[48:49], 0, v[236:237]
	v_lshl_add_u64 v[32:33], v[32:33], 0, v[236:237]
	global_load_ushort v84, v[48:49], off
	global_load_ushort v152, v[32:33], off
	v_lshl_add_u64 v[48:49], v[48:49], 0, v[238:239]
	v_lshl_add_u64 v[32:33], v[32:33], 0, v[238:239]
	global_load_ushort v78, v[48:49], off
	global_load_ushort v147, v[32:33], off
	v_lshl_add_u64 v[48:49], v[48:49], 0, v[236:237]
	v_lshl_add_u64 v[32:33], v[32:33], 0, v[236:237]
	global_load_ushort v79, v[48:49], off
	global_load_ushort v146, v[32:33], off
	v_lshl_add_u64 v[48:49], v[48:49], 0, v[236:237]
	v_lshl_add_u64 v[32:33], v[32:33], 0, v[236:237]
	global_load_ushort v80, v[48:49], off
	global_load_ushort v149, v[32:33], off
	v_lshl_add_u64 v[48:49], v[48:49], 0, v[236:237]
	v_lshl_add_u64 v[32:33], v[32:33], 0, v[236:237]
	global_load_ushort v81, v[48:49], off
	global_load_ushort v148, v[32:33], off
	v_lshl_add_u64 v[48:49], v[48:49], 0, v[238:239]
	v_lshl_add_u64 v[32:33], v[32:33], 0, v[238:239]
	global_load_ushort v90, v[48:49], off
	global_load_ushort v144, v[32:33], off
	v_lshl_add_u64 v[48:49], v[48:49], 0, v[236:237]
	v_lshl_add_u64 v[32:33], v[32:33], 0, v[236:237]
	global_load_ushort v91, v[48:49], off
	global_load_ushort v142, v[32:33], off
	v_lshl_add_u64 v[48:49], v[48:49], 0, v[236:237]
	v_lshl_add_u64 v[32:33], v[32:33], 0, v[236:237]
	global_load_ushort v92, v[48:49], off
	global_load_ushort v145, v[32:33], off
	v_lshl_add_u64 v[48:49], v[48:49], 0, v[236:237]
	v_lshl_add_u64 v[32:33], v[32:33], 0, v[236:237]
	global_load_ushort v93, v[48:49], off
	global_load_ushort v143, v[32:33], off
	v_lshl_add_u64 v[48:49], v[48:49], 0, v[238:239]
	v_lshl_add_u64 v[32:33], v[32:33], 0, v[238:239]
	global_load_ushort v117, v[48:49], off
	global_load_ushort v140, v[32:33], off
	v_lshl_add_u64 v[48:49], v[48:49], 0, v[236:237]
	v_lshl_add_u64 v[32:33], v[32:33], 0, v[236:237]
	global_load_ushort v120, v[48:49], off
	global_load_ushort v138, v[32:33], off
	v_lshl_add_u64 v[48:49], v[48:49], 0, v[236:237]
	v_lshl_add_u64 v[32:33], v[32:33], 0, v[236:237]
	global_load_ushort v121, v[48:49], off
	global_load_ushort v141, v[32:33], off
	v_lshl_add_u64 v[48:49], v[48:49], 0, v[236:237]
	v_lshl_add_u64 v[32:33], v[32:33], 0, v[236:237]
	global_load_ushort v122, v[48:49], off
	global_load_ushort v139, v[32:33], off
	s_branch .Lgf2a_done
.Lgf2a_noq:
	s_waitcnt vmcnt(8)
	global_load_ushort v34, v[48:49], off
	v_lshl_add_u64 v[48:49], v[48:49], 0, v[236:237]
	global_load_ushort v82, v[48:49], off
	v_lshl_add_u64 v[48:49], v[48:49], 0, v[236:237]
	global_load_ushort v83, v[48:49], off
	v_lshl_add_u64 v[48:49], v[48:49], 0, v[236:237]
	global_load_ushort v84, v[48:49], off
	v_lshl_add_u64 v[48:49], v[48:49], 0, v[238:239]
	global_load_ushort v78, v[48:49], off
	v_lshl_add_u64 v[48:49], v[48:49], 0, v[236:237]
	global_load_ushort v79, v[48:49], off
	v_lshl_add_u64 v[48:49], v[48:49], 0, v[236:237]
	global_load_ushort v80, v[48:49], off
	v_lshl_add_u64 v[48:49], v[48:49], 0, v[236:237]
	global_load_ushort v81, v[48:49], off
	v_lshl_add_u64 v[48:49], v[48:49], 0, v[238:239]
	global_load_ushort v90, v[48:49], off
	v_lshl_add_u64 v[48:49], v[48:49], 0, v[236:237]
	global_load_ushort v91, v[48:49], off
	v_lshl_add_u64 v[48:49], v[48:49], 0, v[236:237]
	global_load_ushort v92, v[48:49], off
	v_lshl_add_u64 v[48:49], v[48:49], 0, v[236:237]
	global_load_ushort v93, v[48:49], off
	v_lshl_add_u64 v[48:49], v[48:49], 0, v[238:239]
	global_load_ushort v117, v[48:49], off
	v_lshl_add_u64 v[48:49], v[48:49], 0, v[236:237]
	global_load_ushort v120, v[48:49], off
	v_lshl_add_u64 v[48:49], v[48:49], 0, v[236:237]
	global_load_ushort v121, v[48:49], off
	v_lshl_add_u64 v[48:49], v[48:49], 0, v[236:237]
	global_load_ushort v122, v[48:49], off
; #define LAS __attribute__((address_space(3)))
; __device__ __forceinline__ unsigned f2bf(float f) { unsigned u = __float_as_uint(f); return (u + 0x7fffu + ((u >> 16) & 1u)) >> 16; }
; __device__ __forceinline__ float rdlane_f(float v, int l) { return __builtin_bit_cast(float, __builtin_amdgcn_readlane(__builtin_bit_cast(int, v), l)); }
; __device__ __forceinline__ float gdn_s1(const GdnIn& in, LAS unsigned char* ub, LAS unsigned char* dwb, int w, int lane) {
;     const int fr = lane & 15, kg = lane >> 4, I1 = w >> 1;
;     LAS bf16* AB = (LAS bf16*)ub; LAS bf16* ATT = AB + 4608; LAS bf16* KTT = ATT + 4608; LAS float* GT = (LAS float*)(dwb + 2048);
;     float beta = in.g2.x, cum = in.g2.y;
; #pragma unroll
;     for (int o = 1; o < 64; o <<= 1) { const float t = __shfl_up(cum, o); if (lane >= o) cum += t; }
;     const float cl = rdlane_f(cum, 63);
;     GT[lane] = beta; GT[64 + lane] = cum; GT[128 + lane] = __expf(cum);
;     asm volatile("s_waitcnt lgkmcnt(0)" ::: "memory");
;     { const f32x4 ci = *(const LAS f32x4*)(GT + 64 + 16 * I1 + 4 * kg), bi = *(const LAS f32x4*)(GT + 16 * I1 + 4 * kg);
; #pragma unroll
;       for (int jj = 0; jj < 2; ++jj) { const int J = 2 * (w & 1) + jj;
;           f32x4 ck = (f32x4){0.f, 0.f, 0.f, 0.f}, cq = (f32x4){0.f, 0.f, 0.f, 0.f};
; #pragma unroll
;           for (int s = 0; s < 2; ++s) { ck = __builtin_amdgcn_mfma_f32_16x16x32_bf16(in.ak[s], in.bk[jj][s], ck, 0, 0, 0); cq = __builtin_amdgcn_mfma_f32_16x16x32_bf16(in.aq[s], in.bk[jj][s], cq, 0, 0, 0); }
;           const int j = 16 * J + fr; const float cj = GT[64 + j];
; #pragma unroll
;           for (int e = 0; e < 4; ++e) { const int i = 16 * I1 + 4 * kg + e; const float gm = __expf(fminf(ci[e] - cj, 0.f));
;               AB[i * 72 + j] = (bf16)f2bf(j < i ? bi[e] * ck[e] * gm : 0.f); ATT[i * 72 + j] = (bf16)f2bf(j <= i ? cq[e] * gm : 0.f); } } }
.Lgf2a_done:
.LBB0_1719:
	v_and_b32_e32 v32, 64, v195
	v_add_u32_e32 v33, -1, v195
	v_cmp_lt_i32_e32 vcc, v33, v32
	v_add_u32_e32 v46, -2, v195
	v_add_u32_e32 v67, s42, v54
	v_cndmask_b32_e32 v33, v33, v195, vcc
	v_lshlrev_b32_e32 v125, 2, v33
	ds_bpermute_b32 v33, v125, v113
	v_cmp_gt_i32_e32 vcc, 1, v110
	v_mfma_f32_16x16x32_bf16 v[58:61], v[6:9], v[10:13], 0
	s_movk_i32 s2, 0x48
	v_or_b32_e32 v69, 1, v67
	s_waitcnt lgkmcnt(0)
	v_add_f32_e32 v33, v113, v33
	v_cndmask_b32_e32 v33, v33, v113, vcc
	v_cmp_lt_i32_e32 vcc, v46, v32
	v_or_b32_e32 v70, 2, v67
	s_add_i32 s28, s26, 1
	v_cndmask_b32_e32 v46, v46, v195, vcc
	v_lshlrev_b32_e32 v126, 2, v46
	ds_bpermute_b32 v46, v126, v33
	v_cmp_gt_i32_e32 vcc, 2, v110
	s_mov_b64 s[48:49], -1
	s_waitcnt lgkmcnt(0)
	v_add_f32_e32 v46, v33, v46
	v_cndmask_b32_e32 v33, v46, v33, vcc
	v_add_u32_e32 v46, -4, v195
	v_cmp_lt_i32_e32 vcc, v46, v32
	s_nop 1
	v_cndmask_b32_e32 v46, v46, v195, vcc
	v_lshlrev_b32_e32 v127, 2, v46
	ds_bpermute_b32 v46, v127, v33
	v_cmp_gt_i32_e32 vcc, 4, v110
	s_waitcnt lgkmcnt(0)
	v_add_f32_e32 v46, v33, v46
	v_cndmask_b32_e32 v33, v46, v33, vcc
	v_add_u32_e32 v46, -8, v195
	v_cmp_lt_i32_e32 vcc, v46, v32
	s_nop 1
	v_cndmask_b32_e32 v46, v46, v195, vcc
	v_lshlrev_b32_e32 v128, 2, v46
	ds_bpermute_b32 v46, v128, v33
	v_cmp_gt_i32_e32 vcc, 8, v110
	s_waitcnt lgkmcnt(0)
	v_add_f32_e32 v46, v33, v46
	v_cndmask_b32_e32 v33, v46, v33, vcc
	v_add_u32_e32 v46, -16, v195
	v_cmp_lt_i32_e32 vcc, v46, v32
	s_nop 1
	v_cndmask_b32_e32 v46, v46, v195, vcc
	v_lshlrev_b32_e32 v129, 2, v46
	ds_bpermute_b32 v46, v129, v33
	v_cmp_gt_i32_e32 vcc, 16, v110
	s_waitcnt lgkmcnt(0)
	v_add_f32_e32 v46, v33, v46
	v_cndmask_b32_e32 v33, v46, v33, vcc
	v_subrev_u32_e32 v46, 32, v195
	v_cmp_lt_i32_e32 vcc, v46, v32
	s_nop 1
	v_cndmask_b32_e32 v32, v46, v195, vcc
	v_lshlrev_b32_e32 v130, 2, v32
	ds_bpermute_b32 v32, v130, v33
	v_cmp_gt_i32_e32 vcc, 32, v110
	s_waitcnt lgkmcnt(0)
	v_add_f32_e32 v32, v33, v32
	v_cndmask_b32_e32 v66, v32, v33, vcc
	v_mul_f32_e32 v33, 0x3fb8aa3b, v66
	v_exp_f32_e32 v33, v33
	v_lshl_add_u32 v32, v110, 2, s8
	ds_write2st64_b32 v32, v112, v66 offset0:224 offset1:225
	v_readlane_b32 s36, v66, 63
	ds_write_b32 v32, v33 offset:57856
	s_waitcnt lgkmcnt(0)
	v_lshl_add_u32 v32, v54, 2, s30
	v_mfma_f32_16x16x32_bf16 v[54:57], v[2:5], v[10:13], 0
	ds_read_b128 v[50:53], v32 offset:57600
	ds_read_b128 v[46:49], v32 offset:57344
	v_or_b32_e32 v32, s43, v119
	v_lshl_add_u32 v33, v32, 2, s8
	v_add_u32_e32 v33, 0xe000, v33
	v_mfma_f32_16x16x32_bf16 v[62:65], v[18:21], v[26:29], v[54:57]
	v_cmp_lt_i32_e32 vcc, v32, v67
	s_nop 1
	ds_read2_b32 v[54:55], v33 offset0:64 offset1:80
	v_mfma_f32_16x16x32_bf16 v[56:59], v[22:25], v[26:29], v[58:61]
	s_waitcnt lgkmcnt(0)
	v_sub_f32_e32 v33, v50, v54
	v_min_f32_e32 v33, 0, v33
	v_mul_f32_e32 v33, 0x3fb8aa3b, v33
	v_exp_f32_e32 v33, v33
	v_mul_f32_e32 v60, v46, v62
	v_sub_f32_e32 v50, v50, v55
	v_min_f32_e32 v50, 0, v50
	v_mul_f32_e32 v60, v60, v33
	v_cndmask_b32_e32 v60, 0, v60, vcc
	v_bfe_u32 v61, v60, 16, 1
	v_add3_u32 v62, v60, v61, s81
	v_mad_u64_u32 v[60:61], s[2:3], v67, s2, v[32:33]
	v_cmp_gt_i32_e32 vcc, v32, v67
	v_mul_f32_e32 v33, v56, v33
	v_lshl_add_u32 v68, v60, 1, 0
	v_cndmask_b32_e64 v33, v33, 0, vcc
	v_cvt_pk_bf16_f32 v33, v33, v33
	ds_write_b16 v68, v33 offset:9216
	v_sub_f32_e32 v33, v51, v54
	v_min_f32_e32 v33, 0, v33
	v_mul_f32_e32 v33, 0x3fb8aa3b, v33
	v_exp_f32_e32 v33, v33
	v_mul_f32_e32 v56, v47, v63
	v_mul_f32_e32 v50, 0x3fb8aa3b, v50
	ds_write_b16_d16_hi v68, v62
	v_mul_f32_e32 v56, v56, v33
	v_cndmask_b32_e64 v56, v56, 0, vcc
	v_bfe_u32 v60, v56, 16, 1
	v_mul_f32_e32 v33, v57, v33
	v_cmp_le_i32_e32 vcc, v32, v69
	v_add3_u32 v56, v56, v60, s81
	ds_write_b16_d16_hi v68, v56 offset:144
	v_cndmask_b32_e32 v33, 0, v33, vcc
	v_cvt_pk_bf16_f32 v33, v33, v33
	ds_write_b16 v68, v33 offset:9360
	v_sub_f32_e32 v33, v52, v54
	v_min_f32_e32 v33, 0, v33
	v_mul_f32_e32 v33, 0x3fb8aa3b, v33
	v_exp_f32_e32 v33, v33
	v_mul_f32_e32 v56, v48, v64
	v_cmp_lt_i32_e32 vcc, v32, v70
	v_or_b32_e32 v64, 3, v67
	v_mul_f32_e32 v56, v56, v33
	v_cndmask_b32_e32 v56, 0, v56, vcc
	v_bfe_u32 v57, v56, 16, 1
	v_mul_f32_e32 v33, v58, v33
	v_cmp_le_i32_e32 vcc, v32, v70
	v_add3_u32 v56, v56, v57, s81
	ds_write_b16_d16_hi v68, v56 offset:288
	v_cndmask_b32_e32 v33, 0, v33, vcc
	v_cvt_pk_bf16_f32 v33, v33, v33
	ds_write_b16 v68, v33 offset:9504
	v_sub_f32_e32 v33, v53, v54
	v_min_f32_e32 v33, 0, v33
	v_mul_f32_e32 v33, 0x3fb8aa3b, v33
	v_exp_f32_e32 v33, v33
	v_mul_f32_e32 v54, v49, v65
	v_cmp_lt_i32_e32 vcc, v32, v64
	v_mfma_f32_16x16x32_bf16 v[60:63], v[6:9], v[14:17], 0
	v_mul_f32_e32 v54, v54, v33
	v_cndmask_b32_e32 v54, 0, v54, vcc
	v_bfe_u32 v56, v54, 16, 1
	v_add3_u32 v54, v54, v56, s81
	v_mul_f32_e32 v33, v59, v33
	v_mfma_f32_16x16x32_bf16 v[56:59], v[2:5], v[14:17], 0
	v_cmp_le_i32_e32 vcc, v32, v64
	v_exp_f32_e32 v50, v50
	ds_write_b16_d16_hi v68, v54 offset:432
	v_mfma_f32_16x16x32_bf16 v[56:59], v[18:21], v[36:39], v[56:59]
	v_cndmask_b32_e32 v33, 0, v33, vcc
	v_cvt_pk_bf16_f32 v33, v33, v33
; #define LAS __attribute__((address_space(3)))
; __device__ __forceinline__ unsigned f2bf(float f) { unsigned u = __float_as_uint(f); return (u + 0x7fffu + ((u >> 16) & 1u)) >> 16; }
; __device__ __forceinline__ float gdn_s1(const GdnIn& in, LAS unsigned char* ub, LAS unsigned char* dwb, int w, int lane) {
;     ...
;     { const f32x4 c8a = *(const LAS f32x4*)(GT + 64 + 8 * w), c8b = *(const LAS f32x4*)(GT + 64 + 8 * w + 4);
; #pragma unroll
;       for (int tt = 0; tt < 8; ++tt) KTT[lane * 72 + 8 * w + tt] = (bf16)f2bf(__uint_as_float(in.kt8[tt] << 16) * __expf(cl - (tt < 4 ? c8a[tt & 3] : c8b[tt & 3]))); }
;     asm volatile("s_waitcnt lgkmcnt(0)" ::: "memory");
;     return cl;
; __device__ __forceinline__ void gdn_chain_units(CArgs& a, int chain, LAS unsigned char* lds, int w, int lane, unsigned long long& tacc) {
;     ...
;           gdn_fetch2(a, chain * 36 + n, w, lane, C); const float cl = gdn_s1(A, lds, dwb, w, lane);
;           if (PROBE_PH == 60) tacc += __builtin_amdgcn_s_memrealtime() - tq; if (PROBE_PH == 61) tq = __builtin_amdgcn_s_memrealtime();
;           __syncthreads();
;           if (PROBE_PH == 61) tacc += __builtin_amdgcn_s_memrealtime() - tq; if (PROBE_PH >= 62 && PROBE_PH <= 64) tq = __builtin_amdgcn_s_memrealtime();
;           gdn_fetch(a, chain * 36 + n + 1, w, lane, B); gdn_s23(a, chain * 36 + n, C, lds, dwb, w, lane, cl);
	ds_write_b16 v68, v33 offset:9648
	v_or_b32_e32 v33, 16, v32
	s_nop 2
	s_nop 0
	v_mul_f32_e32 v46, v46, v56
	v_mfma_f32_16x16x32_bf16 v[60:63], v[22:25], v[36:39], v[60:63]
	v_cmp_lt_i32_e32 vcc, v33, v67
	v_mul_f32_e32 v46, v46, v50
	v_mul_f32_e32 v47, v47, v57
	v_cndmask_b32_e32 v46, 0, v46, vcc
	v_cvt_pk_bf16_f32 v46, v46, v46
	ds_write_b16 v68, v46 offset:32
	v_cmp_gt_i32_e32 vcc, v33, v67
	s_nop 0
	v_mul_f32_e32 v46, v60, v50
	v_mul_lo_u32 v54, v110, s75
	v_cndmask_b32_e64 v46, v46, 0, vcc
	v_cvt_pk_bf16_f32 v46, v46, v46
	ds_write_b16 v68, v46 offset:9248
	v_sub_f32_e32 v46, v51, v55
	v_min_f32_e32 v46, 0, v46
	v_mul_f32_e32 v46, 0x3fb8aa3b, v46
	v_exp_f32_e32 v46, v46
	v_lshlrev_b32_e32 v57, 16, v1
	v_lshlrev_b32_e32 v56, 16, v30
	s_mov_b32 s2, 0x7060302
	v_mul_f32_e32 v47, v47, v46
	v_cndmask_b32_e64 v47, v47, 0, vcc
	v_mul_f32_e32 v46, v61, v46
	v_cmp_le_i32_e32 vcc, v33, v69
	v_cvt_pk_bf16_f32 v47, v47, v47
	ds_write_b16 v68, v47 offset:176
	v_cndmask_b32_e32 v46, 0, v46, vcc
	v_cvt_pk_bf16_f32 v46, v46, v46
	ds_write_b16 v68, v46 offset:9392
	v_sub_f32_e32 v46, v52, v55
	v_min_f32_e32 v46, 0, v46
	v_mul_f32_e32 v46, 0x3fb8aa3b, v46
	v_exp_f32_e32 v46, v46
	v_mul_f32_e32 v47, v48, v58
	v_cmp_lt_i32_e32 vcc, v33, v70
	v_mov_b32_e32 v50, s84
	v_mul_f32_e32 v47, v47, v46
	v_cndmask_b32_e32 v47, 0, v47, vcc
	v_mul_f32_e32 v46, v62, v46
	v_cmp_le_i32_e32 vcc, v33, v70
	v_cvt_pk_bf16_f32 v47, v47, v47
	ds_write_b16 v68, v47 offset:320
	v_cndmask_b32_e32 v46, 0, v46, vcc
	v_cvt_pk_bf16_f32 v46, v46, v46
	ds_write_b16 v68, v46 offset:9536
	v_sub_f32_e32 v46, v53, v55
	v_min_f32_e32 v46, 0, v46
	v_mul_f32_e32 v46, 0x3fb8aa3b, v46
	v_exp_f32_e32 v46, v46
	v_mul_f32_e32 v47, v49, v59
	v_cmp_lt_i32_e32 vcc, v33, v64
	v_add_u32_e32 v58, s11, v54
	v_mul_f32_e32 v47, v47, v46
	v_cndmask_b32_e32 v47, 0, v47, vcc
	v_mul_f32_e32 v46, v63, v46
	v_cmp_le_i32_e32 vcc, v33, v64
	v_cvt_pk_bf16_f32 v47, v47, v47
	ds_write_b16 v68, v47 offset:464
	v_cndmask_b32_e32 v46, 0, v46, vcc
	v_cvt_pk_bf16_f32 v46, v46, v46
	ds_write_b16 v68, v46 offset:9680
	ds_read_b128 v[46:49], v50 offset:57600
	ds_read_b128 v[50:53], v50 offset:57616
	v_lshlrev_b32_e32 v55, 16, v31
	v_lshlrev_b32_e32 v54, 16, v40
	s_waitcnt lgkmcnt(1)
	v_sub_f32_e32 v46, s36, v46
	v_sub_f32_e32 v47, s36, v47
	v_sub_f32_e32 v48, s36, v48
	v_sub_f32_e32 v49, s36, v49
	v_mul_f32_e32 v46, 0x3fb8aa3b, v46
	v_mul_f32_e32 v47, 0x3fb8aa3b, v47
	v_mul_f32_e32 v48, 0x3fb8aa3b, v48
	v_mul_f32_e32 v49, 0x3fb8aa3b, v49
	v_exp_f32_e32 v46, v46
	v_exp_f32_e32 v47, v47
	v_exp_f32_e32 v48, v48
	v_exp_f32_e32 v49, v49
	s_waitcnt lgkmcnt(0)
	v_sub_f32_e32 v50, s36, v50
	v_sub_f32_e32 v51, s36, v51
	v_sub_f32_e32 v52, s36, v52
	v_sub_f32_e32 v53, s36, v53
	v_mul_f32_e32 v50, 0x3fb8aa3b, v50
	v_mul_f32_e32 v51, 0x3fb8aa3b, v51
	v_mul_f32_e32 v52, 0x3fb8aa3b, v52
	v_mul_f32_e32 v53, 0x3fb8aa3b, v53
	v_exp_f32_e32 v50, v50
	v_exp_f32_e32 v51, v51
	v_exp_f32_e32 v52, v52
	v_exp_f32_e32 v53, v53
	v_pk_mul_f32 v[46:47], v[46:47], v[56:57]
	v_pk_mul_f32 v[48:49], v[48:49], v[54:55]
	v_bfe_u32 v56, v47, 16, 1
	v_bfe_u32 v54, v49, 16, 1
	v_bfe_u32 v55, v48, 16, 1
	v_bfe_u32 v57, v46, 16, 1
	v_add3_u32 v57, v46, v57, s81
	v_add3_u32 v56, v47, v56, s81
	v_add3_u32 v55, v48, v55, s81
	v_add3_u32 v54, v49, v54, s81
	v_lshlrev_b32_e32 v47, 16, v43
	v_lshlrev_b32_e32 v46, 16, v44
	v_lshlrev_b32_e32 v49, 16, v41
	v_lshlrev_b32_e32 v48, 16, v42
	v_pk_mul_f32 v[48:49], v[50:51], v[48:49]
	v_pk_mul_f32 v[46:47], v[52:53], v[46:47]
	v_bfe_u32 v52, v49, 16, 1
	v_bfe_u32 v50, v47, 16, 1
	v_bfe_u32 v51, v46, 16, 1
	v_bfe_u32 v53, v48, 16, 1
	v_add3_u32 v48, v48, v53, s81
	v_add3_u32 v52, v49, v52, s81
	v_add3_u32 v46, v46, v51, s81
	v_add3_u32 v47, v47, v50, s81
	v_perm_b32 v49, v47, v46, s2
	v_perm_b32 v48, v52, v48, s2
	v_perm_b32 v47, v54, v55, s2
	v_perm_b32 v46, v56, v57, s2
	s_mul_hi_i32 s2, s28, 0x38e38e39
	s_lshr_b32 s3, s2, 31
	s_ashr_i32 s9, s2, 3
	s_add_i32 s9, s9, s3
	s_mul_i32 s2, s9, 36
	s_sub_i32 s2, s28, s2
	ds_write_b128 v58, v[46:49] offset:18432
	s_ashr_i32 s29, s9, 3
	s_and_b32 s27, s9, 1
	s_lshl_b32 s20, s2, 6
	s_waitcnt lgkmcnt(0)
	s_cmp_gt_i32 s2, 3
	s_cselect_b64 s[56:57], -1, 0
	s_and_b64 vcc, exec, s[56:57]
	s_waitcnt lgkmcnt(0)
	s_barrier
	s_waitcnt vmcnt(0)
	v_lshlrev_b32_e32 v151, 16, v151
	v_lshlrev_b32_e32 v150, 16, v150
	v_lshlrev_b32_e32 v153, 16, v153
	v_lshlrev_b32_e32 v152, 16, v152
	v_lshlrev_b32_e32 v147, 16, v147
	v_lshlrev_b32_e32 v146, 16, v146
	v_lshlrev_b32_e32 v149, 16, v149
	v_lshlrev_b32_e32 v148, 16, v148
	v_lshlrev_b32_e32 v144, 16, v144
	v_lshlrev_b32_e32 v142, 16, v142
	v_lshlrev_b32_e32 v145, 16, v145
	v_lshlrev_b32_e32 v143, 16, v143
	v_lshlrev_b32_e32 v140, 16, v140
	v_lshlrev_b32_e32 v138, 16, v138
	v_lshlrev_b32_e32 v141, 16, v141
	v_lshlrev_b32_e32 v139, 16, v139
	s_cbranch_vccz .LBB0_1721
	s_add_i32 s2, s20, 0xffffff00
	s_lshl_b32 s3, s29, 11
	s_sub_i32 s48, 0x8ff, s20
	s_cmp_eq_u32 s27, 0
	s_cselect_b32 s2, s2, s48
	s_add_i32 s2, s3, s2
	s_addk_i32 s2, 0x1000
	s_mov_b64 s[48:49], 0

; __device__ __forceinline__ void gdn_fetch2(CArgs& a, int u, int w, int lane, GdnIn2& in) {
;     const int chain = u / 36, n = u % 36, b = chain >> 3, h = (chain >> 1) & 3, dir = chain & 1;
;     const int r0 = scan_row(b, dir, n * 64), step = dir ? -1 : 1, fr = lane & 15, kg = lane >> 4;
;     const bf16* QBh = (const bf16*)(a.ws + WS_CKD + CD_QB) + h * 64; const bf16* KBh = (const bf16*)(a.ws + WS_CKD + CD_KB) + h * 64; const bf16* VBh = (const bf16*)(a.ws + WS_MIX + MX_DV) + h * 64;
;     const bool isW = w >= 4; const int c0 = 16 * (w & 3);
; #pragma unroll
;     for (int I = 0; I < 4; ++I)
; #pragma unroll
;         for (int e = 0; e < 4; ++e) { const size_t ro = (size_t)(r0 + step * (16 * I + 4 * kg + e)) * 256 + c0 + fr; in.R[I][e] = isW ? (unsigned)KBh[ro] : (unsigned)VBh[ro]; in.Qv[I][e] = isW ? (unsigned)QBh[ro] : 0u; }
; }
.LBB0_1743:
	v_ashrrev_i32_e32 v78, 2, v110
	v_and_b32_e32 v34, -4, v78
	s_lshl_b32 s2, s9, 6
	v_sub_u32_e32 v32, 0, v34
	s_and_b32 s2, s2, 0x180
	v_cndmask_b32_e64 v32, v32, v34, s[52:53]
	s_add_u32 s56, s37, s2
	v_add_u32_e32 v32, s27, v32
	v_and_b32_e32 v106, 15, v110
	s_addc_u32 s57, s72, 0
	v_ashrrev_i32_e32 v33, 31, v32
	v_or_b32_e32 v45, s68, v106
	s_add_u32 s62, s69, s2
	v_lshlrev_b64 v[32:33], 8, v[32:33]
	s_addc_u32 s63, s15, 0
	v_or_b32_e32 v32, v32, v45
	v_mov_b32_e32 v102, 0
	v_mov_b32_e32 v103, 0
	v_mov_b32_e32 v104, 0
	v_mov_b32_e32 v105, 0
	v_mov_b32_e32 v98, 0
	v_mov_b32_e32 v99, 0
	v_mov_b32_e32 v100, 0
	v_mov_b32_e32 v101, 0
	v_mov_b32_e32 v94, 0
	v_mov_b32_e32 v96, 0
	v_mov_b32_e32 v95, 0
	v_mov_b32_e32 v97, 0
	v_mov_b32_e32 v90, 0
	v_mov_b32_e32 v92, 0
	v_mov_b32_e32 v91, 0
	v_mov_b32_e32 v93, 0
	v_mov_b32_e32 v236, 0x200
	v_mov_b32_e32 v240, 0xfffffe00
	v_mov_b32_e32 v238, 0x1a00
	v_mov_b32_e32 v241, 0xffffe600
	v_cndmask_b32_e64 v236, v240, v236, s[52:53]
	v_cndmask_b32_e64 v238, v241, v238, s[52:53]
	v_ashrrev_i32_e32 v237, 31, v236
	v_ashrrev_i32_e32 v239, 31, v238
	v_lshl_add_u64 v[80:81], v[32:33], 1, s[62:63]
	s_and_b64 vcc, exec, s[50:51]
	s_cbranch_vccnz .Lgf2b_noq
	v_lshl_add_u64 v[32:33], v[32:33], 1, s[56:57]
	global_load_ushort v123, v[80:81], off
	global_load_ushort v103, v[32:33], off
	v_lshl_add_u64 v[80:81], v[80:81], 0, v[236:237]
	v_lshl_add_u64 v[32:33], v[32:33], 0, v[236:237]
	global_load_ushort v139, v[80:81], off
	global_load_ushort v102, v[32:33], off
	v_lshl_add_u64 v[80:81], v[80:81], 0, v[236:237]
	v_lshl_add_u64 v[32:33], v[32:33], 0, v[236:237]
	global_load_ushort v141, v[80:81], off
	global_load_ushort v105, v[32:33], off
	v_lshl_add_u64 v[80:81], v[80:81], 0, v[236:237]
	v_lshl_add_u64 v[32:33], v[32:33], 0, v[236:237]
	global_load_ushort v142, v[80:81], off
	global_load_ushort v104, v[32:33], off
	v_lshl_add_u64 v[80:81], v[80:81], 0, v[238:239]
	v_lshl_add_u64 v[32:33], v[32:33], 0, v[238:239]
	global_load_ushort v121, v[80:81], off
	global_load_ushort v99, v[32:33], off
	v_lshl_add_u64 v[80:81], v[80:81], 0, v[236:237]
	v_lshl_add_u64 v[32:33], v[32:33], 0, v[236:237]
	global_load_ushort v122, v[80:81], off
	global_load_ushort v98, v[32:33], off
	v_lshl_add_u64 v[80:81], v[80:81], 0, v[236:237]
	v_lshl_add_u64 v[32:33], v[32:33], 0, v[236:237]
	global_load_ushort v138, v[80:81], off
	global_load_ushort v101, v[32:33], off
	v_lshl_add_u64 v[80:81], v[80:81], 0, v[236:237]
	v_lshl_add_u64 v[32:33], v[32:33], 0, v[236:237]
	global_load_ushort v140, v[80:81], off
	global_load_ushort v100, v[32:33], off
	v_lshl_add_u64 v[80:81], v[80:81], 0, v[238:239]
	v_lshl_add_u64 v[32:33], v[32:33], 0, v[238:239]
	global_load_ushort v107, v[80:81], off
	global_load_ushort v96, v[32:33], off
	v_lshl_add_u64 v[80:81], v[80:81], 0, v[236:237]
	v_lshl_add_u64 v[32:33], v[32:33], 0, v[236:237]
	global_load_ushort v108, v[80:81], off
	global_load_ushort v94, v[32:33], off
	v_lshl_add_u64 v[80:81], v[80:81], 0, v[236:237]
	v_lshl_add_u64 v[32:33], v[32:33], 0, v[236:237]
	global_load_ushort v109, v[80:81], off
	global_load_ushort v97, v[32:33], off
	v_lshl_add_u64 v[80:81], v[80:81], 0, v[236:237]
	v_lshl_add_u64 v[32:33], v[32:33], 0, v[236:237]
	global_load_ushort v117, v[80:81], off
	global_load_ushort v95, v[32:33], off
	v_lshl_add_u64 v[80:81], v[80:81], 0, v[238:239]
	v_lshl_add_u64 v[32:33], v[32:33], 0, v[238:239]
	global_load_ushort v116, v[80:81], off
	global_load_ushort v92, v[32:33], off
	v_lshl_add_u64 v[80:81], v[80:81], 0, v[236:237]
	v_lshl_add_u64 v[32:33], v[32:33], 0, v[236:237]
	global_load_ushort v118, v[80:81], off
	global_load_ushort v90, v[32:33], off
	v_lshl_add_u64 v[80:81], v[80:81], 0, v[236:237]
	v_lshl_add_u64 v[32:33], v[32:33], 0, v[236:237]
	global_load_ushort v119, v[80:81], off
	global_load_ushort v93, v[32:33], off
	v_lshl_add_u64 v[80:81], v[80:81], 0, v[236:237]
	v_lshl_add_u64 v[32:33], v[32:33], 0, v[236:237]
	global_load_ushort v120, v[80:81], off
	global_load_ushort v91, v[32:33], off
	s_branch .Lgf2b_done
.Lgf2b_noq:
	global_load_ushort v123, v[80:81], off
	v_lshl_add_u64 v[80:81], v[80:81], 0, v[236:237]
	global_load_ushort v139, v[80:81], off
	v_lshl_add_u64 v[80:81], v[80:81], 0, v[236:237]
	global_load_ushort v141, v[80:81], off
	v_lshl_add_u64 v[80:81], v[80:81], 0, v[236:237]
	global_load_ushort v142, v[80:81], off
	v_lshl_add_u64 v[80:81], v[80:81], 0, v[238:239]
	global_load_ushort v121, v[80:81], off
	v_lshl_add_u64 v[80:81], v[80:81], 0, v[236:237]
	global_load_ushort v122, v[80:81], off
	v_lshl_add_u64 v[80:81], v[80:81], 0, v[236:237]
	global_load_ushort v138, v[80:81], off
	v_lshl_add_u64 v[80:81], v[80:81], 0, v[236:237]
	global_load_ushort v140, v[80:81], off
	v_lshl_add_u64 v[80:81], v[80:81], 0, v[238:239]
	global_load_ushort v107, v[80:81], off
	v_lshl_add_u64 v[80:81], v[80:81], 0, v[236:237]
	global_load_ushort v108, v[80:81], off
	v_lshl_add_u64 v[80:81], v[80:81], 0, v[236:237]
	global_load_ushort v109, v[80:81], off
	v_lshl_add_u64 v[80:81], v[80:81], 0, v[236:237]
	global_load_ushort v117, v[80:81], off
	v_lshl_add_u64 v[80:81], v[80:81], 0, v[238:239]
	global_load_ushort v116, v[80:81], off
	v_lshl_add_u64 v[80:81], v[80:81], 0, v[236:237]
	global_load_ushort v118, v[80:81], off
	v_lshl_add_u64 v[80:81], v[80:81], 0, v[236:237]
	global_load_ushort v119, v[80:81], off
	v_lshl_add_u64 v[80:81], v[80:81], 0, v[236:237]
	global_load_ushort v120, v[80:81], off
; #define LAS __attribute__((address_space(3)))
; __device__ __forceinline__ unsigned f2bf(float f) { unsigned u = __float_as_uint(f); return (u + 0x7fffu + ((u >> 16) & 1u)) >> 16; }
; __device__ __forceinline__ void gdn_fetch2(CArgs& a, int u, int w, int lane, GdnIn2& in) {
;     const int chain = u / 36, n = u % 36, b = chain >> 3, h = (chain >> 1) & 3, dir = chain & 1;
;     const int r0 = scan_row(b, dir, n * 64), step = dir ? -1 : 1, fr = lane & 15, kg = lane >> 4;
;     const bf16* QBh = (const bf16*)(a.ws + WS_CKD + CD_QB) + h * 64; const bf16* KBh = (const bf16*)(a.ws + WS_CKD + CD_KB) + h * 64; const bf16* VBh = (const bf16*)(a.ws + WS_MIX + MX_DV) + h * 64;
;     const bool isW = w >= 4; const int c0 = 16 * (w & 3);
; #pragma unroll
;     for (int I = 0; I < 4; ++I)
; #pragma unroll
;         for (int e = 0; e < 4; ++e) { const size_t ro = (size_t)(r0 + step * (16 * I + 4 * kg + e)) * 256 + c0 + fr; in.R[I][e] = isW ? (unsigned)KBh[ro] : (unsigned)VBh[ro]; in.Qv[I][e] = isW ? (unsigned)QBh[ro] : 0u; }
; }
; __device__ __forceinline__ float gdn_s1(const GdnIn& in, LAS unsigned char* ub, LAS unsigned char* dwb, int w, int lane) {
;     ...
;     float beta = in.g2.x, cum = in.g2.y;
; #pragma unroll
;     for (int o = 1; o < 64; o <<= 1) { const float t = __shfl_up(cum, o); if (lane >= o) cum += t; }
;     const float cl = rdlane_f(cum, 63);
;     GT[lane] = beta; GT[64 + lane] = cum; GT[128 + lane] = __expf(cum);
;     asm volatile("s_waitcnt lgkmcnt(0)" ::: "memory");
;     { const f32x4 ci = *(const LAS f32x4*)(GT + 64 + 16 * I1 + 4 * kg), bi = *(const LAS f32x4*)(GT + 16 * I1 + 4 * kg);
; #pragma unroll
;       for (int jj = 0; jj < 2; ++jj) { const int J = 2 * (w & 1) + jj;
;           f32x4 ck = (f32x4){0.f, 0.f, 0.f, 0.f}, cq = (f32x4){0.f, 0.f, 0.f, 0.f};
; #pragma unroll
;           for (int s = 0; s < 2; ++s) { ck = __builtin_amdgcn_mfma_f32_16x16x32_bf16(in.ak[s], in.bk[jj][s], ck, 0, 0, 0); cq = __builtin_amdgcn_mfma_f32_16x16x32_bf16(in.aq[s], in.bk[jj][s], cq, 0, 0, 0); }
;           const int j = 16 * J + fr; const float cj = GT[64 + j];
; #pragma unroll
;           for (int e = 0; e < 4; ++e) { const int i = 16 * I1 + 4 * kg + e; const float gm = __expf(fminf(ci[e] - cj, 0.f));
;               AB[i * 72 + j] = (bf16)f2bf(j < i ? bi[e] * ck[e] * gm : 0.f); ATT[i * 72 + j] = (bf16)f2bf(j <= i ? cq[e] * gm : 0.f); } } }
.Lgf2b_done:
.LBB0_1775:
	s_waitcnt vmcnt(32)
	ds_bpermute_b32 v32, v125, v115
	v_cmp_gt_i32_e32 vcc, 1, v110
	s_waitcnt vmcnt(29)
	v_mfma_f32_16x16x32_bf16 v[86:89], v[58:61], v[70:73], 0
	s_movk_i32 s2, 0x48
	s_cmp_gt_u32 s0, 33
	s_waitcnt lgkmcnt(0)
	v_add_f32_e32 v32, v115, v32
	v_cndmask_b32_e32 v32, v32, v115, vcc
	ds_bpermute_b32 v33, v126, v32
	v_cmp_gt_i32_e32 vcc, 2, v110
	v_mfma_f32_16x16x32_bf16 v[70:73], v[46:49], v[70:73], 0
	s_cselect_b64 s[50:51], -1, 0
	s_mov_b64 s[62:63], 0x40000
	s_waitcnt lgkmcnt(0)
	v_add_f32_e32 v33, v32, v33
	v_cndmask_b32_e32 v32, v33, v32, vcc
	ds_bpermute_b32 v33, v127, v32
	v_cmp_gt_i32_e32 vcc, 4, v110
	s_waitcnt vmcnt(25)
	v_mfma_f32_16x16x32_bf16 v[86:89], v[50:53], v[74:77], v[86:89]
	s_waitcnt lgkmcnt(0)
	v_add_f32_e32 v33, v32, v33
	v_cndmask_b32_e32 v32, v33, v32, vcc
	ds_bpermute_b32 v33, v128, v32
	v_cmp_gt_i32_e32 vcc, 8, v110
	v_mfma_f32_16x16x32_bf16 v[70:73], v[54:57], v[74:77], v[70:73]
	s_waitcnt lgkmcnt(0)
	v_add_f32_e32 v33, v32, v33
	v_cndmask_b32_e32 v32, v33, v32, vcc
	ds_bpermute_b32 v33, v129, v32
	v_cmp_gt_i32_e32 vcc, 16, v110
	v_mfma_f32_16x16x32_bf16 v[46:49], v[46:49], v[62:65], 0
	s_waitcnt lgkmcnt(0)
	v_add_f32_e32 v33, v32, v33
	v_cndmask_b32_e32 v32, v33, v32, vcc
	ds_bpermute_b32 v33, v130, v32
	v_cmp_gt_i32_e32 vcc, 32, v110
	v_mfma_f32_16x16x32_bf16 v[58:61], v[58:61], v[62:65], 0
	s_waitcnt lgkmcnt(0)
	v_add_f32_e32 v33, v32, v33
	v_cndmask_b32_e32 v33, v33, v32, vcc
	v_mul_f32_e32 v78, 0x3fb8aa3b, v33
	v_exp_f32_e32 v78, v78
	v_lshl_add_u32 v32, v110, 2, s8
	ds_write2st64_b32 v32, v114, v33 offset0:224 offset1:225
	v_add_u32_e32 v114, s42, v34
	ds_write_b32 v32, v78 offset:57856
	s_waitcnt lgkmcnt(0)
	v_lshl_add_u32 v32, v34, 2, s30
	ds_read_b128 v[82:85], v32 offset:57600
	ds_read_b128 v[78:81], v32 offset:57344
	v_or_b32_e32 v32, s43, v106
	v_lshl_add_u32 v34, v32, 2, s8
	v_add_u32_e32 v34, 0xe000, v34
	ds_read2_b32 v[74:75], v34 offset0:64 offset1:80
	s_waitcnt lgkmcnt(1)
	v_mul_f32_e32 v76, v78, v86
	v_cmp_lt_i32_e32 vcc, v32, v114
	s_waitcnt vmcnt(24)
	v_mfma_f32_16x16x32_bf16 v[46:49], v[54:57], v[66:69], v[46:49]
	v_readlane_b32 s9, v33, 63
	s_waitcnt lgkmcnt(0)
	v_sub_f32_e32 v34, v82, v74
	v_min_f32_e32 v34, 0, v34
	v_mul_f32_e32 v34, 0x3fb8aa3b, v34
	v_exp_f32_e32 v34, v34
	v_sub_f32_e32 v54, v82, v75
	v_min_f32_e32 v54, 0, v54
	v_mfma_f32_16x16x32_bf16 v[50:53], v[50:53], v[66:69], v[58:61]
	v_mul_f32_e32 v76, v76, v34
	v_cndmask_b32_e32 v76, 0, v76, vcc
	v_cmp_gt_i32_e32 vcc, v32, v114
	v_mul_f32_e32 v34, v70, v34
	s_nop 0
	v_cndmask_b32_e64 v34, v34, 0, vcc
	v_cvt_pk_bf16_f32 v86, v76, v76
	v_mad_u64_u32 v[76:77], s[2:3], v114, s2, v[32:33]
	v_lshl_add_u32 v76, v76, 1, 0
	v_cvt_pk_bf16_f32 v34, v34, v34
	ds_write_b16 v76, v34 offset:36864
	v_sub_f32_e32 v34, v83, v74
	v_min_f32_e32 v34, 0, v34
	v_mul_f32_e32 v34, 0x3fb8aa3b, v34
	v_exp_f32_e32 v34, v34
	v_mul_f32_e32 v77, v79, v87
	v_or_b32_e32 v70, 1, v114
	ds_write_b16 v76, v86 offset:27648
	v_mul_f32_e32 v77, v77, v34
	v_cndmask_b32_e64 v77, v77, 0, vcc
	v_mul_f32_e32 v34, v71, v34
	v_cmp_le_i32_e32 vcc, v32, v70
	v_cvt_pk_bf16_f32 v77, v77, v77
	s_nop 0
	v_cndmask_b32_e32 v34, 0, v34, vcc
	v_cvt_pk_bf16_f32 v34, v34, v34
	ds_write_b16 v76, v34 offset:37008
	v_sub_f32_e32 v34, v84, v74
	v_min_f32_e32 v34, 0, v34
	v_mul_f32_e32 v34, 0x3fb8aa3b, v34
	v_exp_f32_e32 v34, v34
	ds_write_b16 v76, v77 offset:27792
	v_or_b32_e32 v71, 2, v114
	v_mul_f32_e32 v77, v80, v88
	v_cmp_lt_i32_e32 vcc, v32, v71
	v_mul_f32_e32 v77, v77, v34
	v_mul_f32_e32 v34, v72, v34
	v_cndmask_b32_e32 v77, 0, v77, vcc
	v_cmp_le_i32_e32 vcc, v32, v71
	v_mul_f32_e32 v54, 0x3fb8aa3b, v54
	v_exp_f32_e32 v54, v54
	v_cndmask_b32_e32 v34, 0, v34, vcc
	v_cvt_pk_bf16_f32 v34, v34, v34
	ds_write_b16 v76, v34 offset:37152
	v_sub_f32_e32 v34, v85, v74
	v_min_f32_e32 v34, 0, v34
	v_mul_f32_e32 v34, 0x3fb8aa3b, v34
	v_exp_f32_e32 v34, v34
	v_or_b32_e32 v72, 3, v114
	v_mul_f32_e32 v74, v81, v89
	v_cmp_lt_i32_e32 vcc, v32, v72
	v_mul_f32_e32 v74, v74, v34
	v_mul_f32_e32 v34, v73, v34
	v_cndmask_b32_e32 v74, 0, v74, vcc
	v_cmp_le_i32_e32 vcc, v32, v72
	v_mul_f32_e32 v50, v78, v50
	v_mul_f32_e32 v50, v50, v54
	v_cndmask_b32_e32 v34, 0, v34, vcc
	v_bfe_u32 v73, v34, 16, 1
	v_add3_u32 v34, v34, v73, s81
	ds_write_b16_d16_hi v76, v34 offset:37296
	v_or_b32_e32 v34, 16, v32
	v_cmp_lt_i32_e32 vcc, v34, v114
	v_mul_f32_e32 v46, v46, v54
	v_bfe_u32 v86, v77, 16, 1
	v_cndmask_b32_e32 v50, 0, v50, vcc
	v_cmp_gt_i32_e32 vcc, v34, v114
	v_cvt_pk_bf16_f32 v50, v50, v50
	ds_write_b16 v76, v50 offset:27680
	v_cndmask_b32_e64 v46, v46, 0, vcc
	v_cvt_pk_bf16_f32 v46, v46, v46
	ds_write_b16 v76, v46 offset:36896
	v_sub_f32_e32 v46, v83, v75
	v_min_f32_e32 v46, 0, v46
	v_mul_f32_e32 v46, 0x3fb8aa3b, v46
	v_exp_f32_e32 v46, v46
	v_mul_f32_e32 v50, v79, v51
	v_add3_u32 v77, v77, v86, s81
	ds_write_b16_d16_hi v76, v77 offset:27936
	v_mul_f32_e32 v50, v50, v46
	v_cndmask_b32_e64 v50, v50, 0, vcc
	v_mul_f32_e32 v46, v47, v46
	v_cmp_le_i32_e32 vcc, v34, v70
	v_cvt_pk_bf16_f32 v50, v50, v50
	s_nop 0
	v_cndmask_b32_e32 v46, 0, v46, vcc
	v_cvt_pk_bf16_f32 v46, v46, v46
	ds_write_b16 v76, v46 offset:37040
	v_sub_f32_e32 v46, v84, v75
	v_min_f32_e32 v46, 0, v46
	v_mul_f32_e32 v46, 0x3fb8aa3b, v46
	v_exp_f32_e32 v46, v46
	v_mul_f32_e32 v47, v80, v52
	v_cmp_lt_i32_e32 vcc, v34, v71
	ds_write_b16 v76, v50 offset:27824
	v_mul_f32_e32 v47, v47, v46
	v_cndmask_b32_e32 v47, 0, v47, vcc
	v_mul_f32_e32 v46, v48, v46
	v_cmp_le_i32_e32 vcc, v34, v71
	v_cvt_pk_bf16_f32 v47, v47, v47
	ds_write_b16 v76, v47 offset:27968
	v_cndmask_b32_e32 v46, 0, v46, vcc
	v_cvt_pk_bf16_f32 v46, v46, v46
	ds_write_b16 v76, v46 offset:37184
	v_sub_f32_e32 v46, v85, v75
	v_min_f32_e32 v46, 0, v46
	v_mul_f32_e32 v46, 0x3fb8aa3b, v46
	v_exp_f32_e32 v46, v46
	v_mul_f32_e32 v47, v81, v53
	v_cmp_lt_i32_e32 vcc, v34, v72
	v_bfe_u32 v77, v74, 16, 1
	v_mul_f32_e32 v47, v47, v46
	v_cndmask_b32_e32 v47, 0, v47, vcc
	v_mul_f32_e32 v46, v49, v46
	v_cmp_le_i32_e32 vcc, v34, v72
	v_cvt_pk_bf16_f32 v47, v47, v47
	ds_write_b16 v76, v47 offset:28112
	v_cndmask_b32_e32 v46, 0, v46, vcc
	v_add3_u32 v74, v74, v77, s81
	v_cvt_pk_bf16_f32 v46, v46, v46
	ds_write_b16_d16_hi v76, v74 offset:28080
	ds_write_b16 v76, v46 offset:37328
	v_mov_b32_e32 v33, s84
	ds_read_b128 v[46:49], v33 offset:57600
	ds_read_b128 v[50:53], v33 offset:57616
	s_waitcnt vmcnt(20)
; #define LAS __attribute__((address_space(3)))
; __device__ __forceinline__ unsigned f2bf(float f) { unsigned u = __float_as_uint(f); return (u + 0x7fffu + ((u >> 16) & 1u)) >> 16; }
; __device__ __forceinline__ float gdn_s1(const GdnIn& in, LAS unsigned char* ub, LAS unsigned char* dwb, int w, int lane) {
;     ...
;     { const f32x4 c8a = *(const LAS f32x4*)(GT + 64 + 8 * w), c8b = *(const LAS f32x4*)(GT + 64 + 8 * w + 4);
; #pragma unroll
;       for (int tt = 0; tt < 8; ++tt) KTT[lane * 72 + 8 * w + tt] = (bf16)f2bf(__uint_as_float(in.kt8[tt] << 16) * __expf(cl - (tt < 4 ? c8a[tt & 3] : c8b[tt & 3]))); }
;     asm volatile("s_waitcnt lgkmcnt(0)" ::: "memory");
; __device__ __forceinline__ void gdn_chain_units(CArgs& a, int chain, LAS unsigned char* lds, int w, int lane, unsigned long long& tacc) {
;     ...
;         { gdn_fetch2(a, chain * 36 + n + 1, w, lane, C); const float cl = gdn_s1(B, lds + 27648, dwb, w, lane); __syncthreads(); if (n + 2 < 36) gdn_fetch(a, chain * 36 + n + 2, w, lane, A); gdn_s23(a, chain * 36 + n + 1, C, lds + 27648, dwb, w, lane, cl); }
	v_lshlrev_b32_e32 v55, 16, v137
	v_lshlrev_b32_e32 v54, 16, v135
	v_lshlrev_b32_e32 v57, 16, v133
	s_waitcnt lgkmcnt(1)
	v_sub_f32_e32 v46, s9, v46
	v_sub_f32_e32 v47, s9, v47
	v_sub_f32_e32 v48, s9, v48
	v_sub_f32_e32 v49, s9, v49
	v_mul_f32_e32 v46, 0x3fb8aa3b, v46
	v_mul_f32_e32 v47, 0x3fb8aa3b, v47
	v_mul_f32_e32 v48, 0x3fb8aa3b, v48
	v_mul_f32_e32 v49, 0x3fb8aa3b, v49
	v_exp_f32_e32 v46, v46
	v_exp_f32_e32 v47, v47
	v_exp_f32_e32 v48, v48
	v_exp_f32_e32 v49, v49
	s_waitcnt lgkmcnt(0)
	v_sub_f32_e32 v50, s9, v50
	v_sub_f32_e32 v51, s9, v51
	v_sub_f32_e32 v52, s9, v52
	v_sub_f32_e32 v53, s9, v53
	v_mul_f32_e32 v50, 0x3fb8aa3b, v50
	v_mul_f32_e32 v51, 0x3fb8aa3b, v51
	v_mul_f32_e32 v52, 0x3fb8aa3b, v52
	v_mul_f32_e32 v53, 0x3fb8aa3b, v53
	v_lshlrev_b32_e32 v56, 16, v131
	v_exp_f32_e32 v50, v50
	v_exp_f32_e32 v51, v51
	v_exp_f32_e32 v52, v52
	v_exp_f32_e32 v53, v53
	v_pk_mul_f32 v[46:47], v[46:47], v[56:57]
	v_pk_mul_f32 v[48:49], v[48:49], v[54:55]
	v_bfe_u32 v56, v47, 16, 1
	v_bfe_u32 v54, v49, 16, 1
	v_bfe_u32 v55, v48, 16, 1
	v_bfe_u32 v57, v46, 16, 1
	v_add3_u32 v57, v46, v57, s81
	v_add3_u32 v56, v47, v56, s81
	v_add3_u32 v55, v48, v55, s81
	v_add3_u32 v54, v49, v54, s81
	s_waitcnt vmcnt(16)
	v_lshlrev_b32_e32 v47, 16, v136
	v_lshlrev_b32_e32 v46, 16, v134
	v_lshlrev_b32_e32 v49, 16, v132
	v_lshlrev_b32_e32 v48, 16, v111
	v_pk_mul_f32 v[48:49], v[50:51], v[48:49]
	v_pk_mul_f32 v[46:47], v[52:53], v[46:47]
	v_bfe_u32 v52, v49, 16, 1
	v_bfe_u32 v50, v47, 16, 1
	v_bfe_u32 v51, v46, 16, 1
	v_bfe_u32 v53, v48, 16, 1
	v_mul_lo_u32 v33, v110, s75
	v_add3_u32 v48, v48, v53, s81
	v_add3_u32 v52, v49, v52, s81
	v_add3_u32 v46, v46, v51, s81
	v_add3_u32 v47, v47, v50, s81
	s_mov_b32 s2, 0x7060302
	v_add_u32_e32 v33, s11, v33
	v_perm_b32 v49, v47, v46, s2
	v_perm_b32 v48, v52, v48, s2
	v_perm_b32 v47, v54, v55, s2
	v_perm_b32 v46, v56, v57, s2
	ds_write_b128 v33, v[46:49] offset:46080
	s_waitcnt lgkmcnt(0)
	s_and_b64 vcc, exec, s[50:51]
	s_waitcnt lgkmcnt(0)
	s_barrier
	s_waitcnt vmcnt(0)
	v_lshlrev_b32_e32 v103, 16, v103
	v_lshlrev_b32_e32 v102, 16, v102
	v_lshlrev_b32_e32 v105, 16, v105
	v_lshlrev_b32_e32 v104, 16, v104
	v_lshlrev_b32_e32 v99, 16, v99
	v_lshlrev_b32_e32 v98, 16, v98
	v_lshlrev_b32_e32 v101, 16, v101
	v_lshlrev_b32_e32 v100, 16, v100
	v_lshlrev_b32_e32 v96, 16, v96
	v_lshlrev_b32_e32 v94, 16, v94
	v_lshlrev_b32_e32 v97, 16, v97
	v_lshlrev_b32_e32 v95, 16, v95
	v_lshlrev_b32_e32 v92, 16, v92
	v_lshlrev_b32_e32 v90, 16, v90
	v_lshlrev_b32_e32 v93, 16, v93
	v_lshlrev_b32_e32 v91, 16, v91
	s_cbranch_vccnz .LBB0_1781
	s_add_i32 s2, s26, 2
	s_mul_hi_i32 s3, s2, 0x38e38e39
	s_lshr_b32 s20, s3, 31
	s_ashr_i32 s3, s3, 3
	s_add_i32 s3, s3, s20
	s_mul_i32 s20, s3, 36
	s_sub_i32 s2, s2, s20
	s_ashr_i32 s36, s3, 3
	s_and_b32 s20, s3, 1
	s_lshl_b32 s29, s2, 6
	s_cmp_gt_i32 s2, 3
	s_mov_b64 s[26:27], -1
	s_cbranch_scc0 .LBB0_1778
	s_add_i32 s2, s29, 0xffffff00
	s_lshl_b32 s26, s36, 11
	s_sub_i32 s27, 0x8ff, s29
	s_cmp_eq_u32 s20, 0
	s_cselect_b32 s2, s2, s27
	s_add_i32 s2, s26, s2
	s_addk_i32 s2, 0x1000
	s_mov_b64 s[26:27], 0
